# attention K tiles: coalesced LDS-DMA source mapping (8 lanes per key row) with an XOR-swizzled row-major LDS image
# speedup vs baseline: 1.0017x; 1.0017x over previous
; template <class BIAS>
; __device__ __forceinline__ void attn_tiles(char* shm, const UnitIO& io, int t_begin, int t_end, const BIAS& B, int tid) {
;     ...
;     const bf16* ksrc = io.K0 + (long)lane * io.kstride + wid * 8;
;     const bf16* vsrc = io.V0 + (long)(16 * (wid & 3) + (lane >> 2)) * io.kstride + (wid >> 2) * 32 + (lane & 3) * 8;
;     const unsigned kdst = lds0 + LDS_K + wid * 1024, vdst = lds0 + LDS_V + wid * 1024;
;     const long tstep = 64 * io.kstride;
;     ...
;     const lds_cptr shm3 = (lds_cptr)shm;
;     const lds_cptr kp0 = shm3 + LDS_K + hi * 1024 + r32 * 16;
;     const lds_cptr vp0 = shm3 + LDS_V + ((lane >> 4) & 1) * 32 + (lane & 3) * 8 + (4 * hi + ((lane & 15) >> 2)) * 64;
; __device__ __forceinline__ void moba_unit(Frame& F, const AttnBufs& A, int b, int h, int qb) {
;     ...
;     att::BiasMoba B; B.slope2 = exp2f(-8.0f * (float)(7 + h) / 10.0f) * LOG2E; B.qrel = w * 32 + r32; B.tqf = (float)(qb * 256 + B.qrel); B.hi = hi; B.w = w; B.nb0 = 4 * qb; B.selmask = selmask; B.u = 32 * (w & 1) + r32 - 4 * hi;
.LBB0_274:
	s_and_b64 vcc, exec, s[0:1]
	s_cbranch_vccz .LBB0_316
	v_readlane_b32 s0, v254, 27
	s_cmp_gt_i32 s0, 0
	s_mov_b64 s[0:1], -1
	s_cbranch_scc0 .LBB0_394
	v_readlane_b32 s100, v253, 15
	v_and_b32_e32 v248, 31, v214
	v_lshlrev_b32_e32 v248, 7, v248
	v_lshrrev_b32_e32 v249, 5, v214
	v_bfe_u32 v250, v214, 1, 3
	v_xor_b32_e32 v251, v249, v250
	v_lshl_add_u32 v240, v251, 4, v248
	v_add_u32_e32 v251, 2, v249
	v_xor_b32_e32 v251, v251, v250
	v_lshl_add_u32 v241, v251, 4, v248
	v_add_u32_e32 v251, 4, v249
	v_xor_b32_e32 v251, v251, v250
	v_lshl_add_u32 v242, v251, 4, v248
	v_add_u32_e32 v251, 6, v249
	v_xor_b32_e32 v251, v251, v250
	v_lshl_add_u32 v243, v251, 4, v248
	v_lshrrev_b32_e32 v248, 3, v214
	s_lshl_b32 s101, s100, 3
	v_add_u32_e32 v248, s101, v248
	v_sub_u32_e32 v246, v248, v214
	v_bfe_u32 v249, v248, 1, 3
	v_and_b32_e32 v250, 7, v214
	v_xor_b32_e32 v249, v250, v249
	v_subrev_u32_e32 v249, s100, v249
	v_lshlrev_b32_e32 v247, 4, v249
	v_lshl_add_u32 v244, v246, 11, v247
	v_ashrrev_i32_e32 v245, 31, v244
	v_readlane_b32 s0, v254, 13
	s_mov_b32 s6, s0
	s_ashr_i32 s34, s0, 5
	s_and_b32 s0, s0, 24
	s_sub_i32 s0, 0xffffffc8, s0
	v_cvt_f32_i32_e32 v0, s0
	v_readlane_b32 s1, v254, 14
	s_and_b32 s0, s6, 31
	s_mov_b32 s2, 0x41200000
	v_writelane_b32 v254, s0, 30
	s_mov_b32 s3, 0x41300000
	s_waitcnt vmcnt(0)
	v_div_scale_f32 v2, s[0:1], s2, s2, v0
	v_rcp_f32_e32 v3, v2
	s_and_b32 s0, s6, 7
	v_writelane_b32 v254, s0, 31
	s_xor_b32 s0, s0, 15
	v_fma_f32 v4, -v2, v3, 1.0
	v_fmac_f32_e32 v3, v4, v3
	v_div_scale_f32 v4, vcc, v0, s2, v0
	v_mul_f32_e32 v5, v4, v3
	v_fma_f32 v6, -v2, v5, v4
	v_fmac_f32_e32 v5, v6, v3
	v_fma_f32 v2, -v2, v5, v4
	v_div_fmas_f32 v2, v2, v3, v5
	v_writelane_b32 v254, s0, 33
	v_div_fixup_f32 v0, v2, s2, v0
	s_mov_b32 s0, 0xc2fc0000
	v_cmp_gt_f32_e32 vcc, s0, v0
	s_ashr_i32 s35, s34, 31
	s_bfe_u32 s4, s6, 0x20003
	v_cndmask_b32_e32 v2, 0, v224, vcc
	v_add_f32_e32 v0, v0, v2
	v_exp_f32_e32 v0, v0
	s_lshl_b64 s[6:7], s[34:35], 12
	s_and_b64 s[0:1], vcc, exec
	s_cselect_b32 s0, 0xffffffc0, 0
	v_ldexp_f32 v0, v0, s0
	s_lshl_b32 s0, s34, 6
	v_mul_f32_e32 v115, 0x3fb8aa3b, v0
	s_or_b32 s21, s0, s4
	s_mov_b32 s0, 2.0
	v_mov_b32_e32 v0, v115
	s_mov_b32 s1, 0x40400000
	v_pk_mul_f32 v[118:119], v[0:1], s[0:1] op_sel_hi:[0,1]
	s_mov_b32 s0, 0x41000000
	s_mov_b32 s1, 0x41100000
	v_pk_mul_f32 v[120:121], v[0:1], s[0:1] op_sel_hi:[0,1]
	s_mov_b32 s0, 0x41800000
	s_mov_b32 s1, 0x41880000
	v_pk_mul_f32 v[124:125], v[0:1], s[0:1] op_sel_hi:[0,1]
	s_mov_b32 s0, 0x41900000
	s_mov_b32 s1, 0x41980000
	v_pk_mul_f32 v[126:127], v[0:1], s[0:1] op_sel_hi:[0,1]
	s_mov_b32 s0, 0x41c00000
	s_mov_b32 s1, 0x41c80000
	v_pk_mul_f32 v[128:129], v[0:1], s[0:1] op_sel_hi:[0,1]
	s_mov_b32 s0, 0x41d00000
	v_pk_mul_f32 v[122:123], v[0:1], s[2:3] op_sel_hi:[0,1]
	s_mov_b32 s1, 0x41d80000
	s_lshl_b32 s2, s72, 5
	v_pk_mul_f32 v[140:141], v[0:1], s[0:1] op_sel_hi:[0,1]
	s_ashr_i32 s0, s2, 31
	v_writelane_b32 v254, s72, 35
	s_add_u32 s1, s6, s2
	v_writelane_b32 v254, s1, 36
	v_writelane_b32 v254, s6, 38
	s_addc_u32 s0, s7, s0
	s_mul_i32 s1, s34, 0x1800000
	v_writelane_b32 v254, s7, 39
	v_writelane_b32 v254, s0, 40
	s_mul_hi_i32 s0, s34, 0x1800000
	s_add_u32 s20, s74, s1
	s_addc_u32 s22, s75, s0
	s_add_u32 s0, s20, 0x8000000
	s_addc_u32 s1, s22, 0
	s_lshl_b32 s33, s4, 7
	v_writelane_b32 v254, s0, 42
	s_add_u32 s0, s0, s33
	v_writelane_b32 v254, s0, 43
	v_writelane_b32 v254, s1, 45
	s_addc_u32 s0, s1, 0
	v_and_b32_e32 v146, 31, v232
	v_writelane_b32 v254, s0, 46
	v_or_b32_e32 v143, s2, v146
	v_writelane_b32 v254, s2, 48
	v_and_or_b32 v147, s2, 32, v146
	s_add_u32 s2, s20, 0x8800000
	s_addc_u32 s3, s22, 0
	s_lshl_b64 s[0:1], s[34:35], 23
	v_writelane_b32 v254, s2, 49
	s_add_u32 s2, s2, s0
	v_writelane_b32 v254, s3, 50
	s_addc_u32 s3, s3, s1
	s_add_u32 s4, s2, s33
	v_writelane_b32 v254, s2, 51
	s_addc_u32 s5, s3, 0
	v_lshlrev_b32_e32 v130, 3, v232
	v_writelane_b32 v254, s3, 52
	s_add_u32 s2, s20, 0x9000000
	s_addc_u32 s3, s22, 0
	s_add_u32 s0, s2, s0
	s_addc_u32 s1, s3, s1
	v_writelane_b32 v254, s2, 53
	s_add_u32 s30, s0, s33
	v_writelane_b32 v254, s3, 54
	s_addc_u32 s31, s1, 0
	s_ashr_i32 s73, s28, 7
	v_writelane_b32 v254, s0, 55
	s_add_u32 s2, s20, 0x9800000
	v_writelane_b32 v254, s1, 57
	s_addc_u32 s3, s22, 0
	v_writelane_b32 v254, s2, 59
	s_add_u32 s2, s2, s33
	v_lshrrev_b32_e32 v131, 5, v194
	v_and_b32_e32 v144, 24, v130
	v_lshlrev_b32_e32 v0, 1, v232
	v_lshlrev_b32_e32 v7, 4, v232
	s_addc_u32 s25, s3, 0
	s_lshl_b64 s[22:23], s[34:35], 25
	v_lshlrev_b32_e32 v6, 4, v146
; template <class BIAS>
; __device__ __forceinline__ void attn_tiles(char* shm, const UnitIO& io, int t_begin, int t_end, const BIAS& B, int tid) {
;     ...
;     const bf16* ksrc = io.K0 + (long)lane * io.kstride + wid * 8;
;     const bf16* vsrc = io.V0 + (long)(16 * (wid & 3) + (lane >> 2)) * io.kstride + (wid >> 2) * 32 + (lane & 3) * 8;
;     const unsigned kdst = lds0 + LDS_K + wid * 1024, vdst = lds0 + LDS_V + wid * 1024;
;     const long tstep = 64 * io.kstride;
;     ...
;     const lds_cptr shm3 = (lds_cptr)shm;
;     const lds_cptr kp0 = shm3 + LDS_K + hi * 1024 + r32 * 16;
;     const lds_cptr vp0 = shm3 + LDS_V + ((lane >> 4) & 1) * 32 + (lane & 3) * 8 + (4 * hi + ((lane & 15) >> 2)) * 64;
;     float* wsf = (float*)(shm + LDS_WS) + wid * 64;
; __device__ __forceinline__ void moba_unit(Frame& F, const AttnBufs& A, int b, int h, int qb) {
;     ...
;     att::BiasMoba B; B.slope2 = exp2f(-8.0f * (float)(7 + h) / 10.0f) * LOG2E; B.qrel = w * 32 + r32; B.tqf = (float)(qb * 256 + B.qrel); B.hi = hi; B.w = w; B.nb0 = 4 * qb; B.selmask = selmask; B.u = 32 * (w & 1) + r32 - 4 * hi;
	v_and_or_b32 v0, v0, 32, v144
	v_lshlrev_b32_e32 v179, 8, v131
	v_and_b32_e32 v7, 0xc0, v7
	s_or_b32 s20, s22, s33
	v_or3_b32 v180, v0, v179, v7
	v_lshl_or_b32 v181, v131, 10, v6
	v_lshlrev_b32_e32 v6, 2, v194
	v_mov_b32_e32 v7, v1
	s_add_u32 s36, s74, s20
	v_bfe_u32 v3, v232, 5, 1
	v_lshl_add_u64 v[6:7], s[74:75], 0, v[6:7]
	s_mov_b64 s[0:1], 0x3700000
	s_addc_u32 s37, s75, s23
	v_lshlrev_b32_e32 v145, 2, v3
	v_lshl_add_u64 v[158:159], v[6:7], 0, s[0:1]
	s_add_u32 s20, s74, s33
	v_and_b32_e32 v6, 3, v232
	v_sub_u32_e32 v5, v147, v145
	v_writelane_b32 v255, s74, 1
	s_addc_u32 s33, s75, 0
	v_lshlrev_b32_e32 v6, 4, v6
	v_mov_b32_e32 v7, v1
	s_add_u32 s22, s20, s22
	v_cmp_gt_i32_e64 s[34:35], 57, v5
	v_lshl_add_u64 v[6:7], s[36:37], 0, v[6:7]
	v_cmp_gt_i32_e64 s[36:37], 58, v5
	v_cmp_gt_i32_e64 s[28:29], 56, v5
	s_addc_u32 s23, s33, s23
	s_and_b64 s[40:41], s[36:37], s[34:35]
	v_cmp_gt_i32_e64 s[26:27], 51, v5
	s_and_b64 s[42:43], s[40:41], s[28:29]
	v_cmp_gt_i32_e64 s[46:47], 50, v5
	s_and_b64 s[44:45], s[42:43], s[26:27]
	v_cmp_gt_i32_e64 s[48:49], 49, v5
	s_and_b64 s[46:47], s[44:45], s[46:47]
	v_cmp_gt_i32_e64 s[50:51], 48, v5
	s_and_b64 s[48:49], s[46:47], s[48:49]
	v_cmp_gt_i32_e64 s[16:17], 43, v5
	s_and_b64 s[50:51], s[48:49], s[50:51]
	v_cmp_gt_i32_e64 s[12:13], 42, v5
	s_and_b64 s[52:53], s[50:51], s[16:17]
	v_cmp_gt_i32_e64 s[10:11], 41, v5
	s_and_b64 s[54:55], s[52:53], s[12:13]
	v_lshlrev_b32_e32 v0, 11, v194
	v_cmp_gt_i32_e64 s[6:7], 40, v5
	s_and_b64 s[56:57], s[54:55], s[10:11]
	v_lshl_add_u64 v[156:157], s[4:5], 0, v[0:1]
	v_cmp_gt_i32_e64 s[4:5], 35, v5
	v_cmp_gt_i32_e64 s[68:69], 26, v5
	v_cmp_gt_i32_e64 s[38:39], 27, v5
	s_and_b64 s[58:59], s[56:57], s[6:7]
	v_cmp_gt_i32_e64 s[62:63], 34, v5
	v_cmp_gt_i32_e64 s[18:19], 25, v5
	s_and_b64 s[60:61], s[58:59], s[4:5]
	s_and_b64 s[68:69], s[38:39], s[68:69]
	v_cmp_gt_i32_e64 s[0:1], 33, v5
	v_cmp_gt_i32_e64 s[14:15], 24, v5
	s_and_b64 s[62:63], s[60:61], s[62:63]
	s_and_b64 s[70:71], s[68:69], s[18:19]
	v_cmp_gt_i32_e32 vcc, 32, v5
	v_cmp_gt_i32_e64 s[8:9], 19, v5
	s_and_b64 s[64:65], s[62:63], s[0:1]
	s_and_b64 s[18:19], s[70:71], s[14:15]
	v_writelane_b32 v255, s75, 2
	s_and_b64 s[66:67], s[64:65], vcc
	s_and_b64 s[74:75], s[18:19], s[8:9]
	v_cmp_gt_i32_e32 vcc, 18, v5
	s_and_b64 s[76:77], s[74:75], vcc
	v_cmp_gt_i32_e32 vcc, 17, v5
	s_and_b64 s[78:79], s[76:77], vcc
	v_cmp_gt_i32_e32 vcc, 16, v5
	s_and_b64 s[80:81], s[78:79], vcc
	v_cmp_gt_i32_e32 vcc, 11, v5
	s_and_b64 s[82:83], s[80:81], vcc
	v_cmp_gt_i32_e32 vcc, 10, v5
	v_writelane_b32 v254, s2, 61
	s_and_b64 s[84:85], s[82:83], vcc
	v_cmp_gt_i32_e32 vcc, 9, v5
	v_writelane_b32 v254, s3, 63
	s_and_b64 s[2:3], s[84:85], vcc
	v_cmp_gt_i32_e32 vcc, 8, v5
	s_and_b64 s[88:89], s[2:3], vcc
	v_cmp_gt_i32_e32 vcc, 3, v5
	v_lshrrev_b32_e32 v182, 3, v194
	s_and_b64 s[90:91], s[88:89], vcc
	v_cmp_gt_i32_e32 vcc, 2, v5
	v_lshl_add_u64 v[8:9], s[22:23], 0, v[0:1]
	v_or_b32_e32 v184, 8, v182
	v_or_b32_e32 v186, 16, v182
	v_or_b32_e32 v188, 24, v182
	s_mov_b64 s[22:23], 0x9060000
	s_and_b64 s[92:93], s[90:91], vcc
	v_cmp_gt_i32_e32 vcc, 1, v5
	v_cmp_gt_u32_e64 s[4:5], 32, v194
	v_mul_f32_e32 v116, 0x42000000, v115
	v_lshlrev_b32_e32 v2, 10, v146
	v_lshlrev_b32_e32 v4, 3, v3
	v_lshrrev_b32_e32 v178, 2, v194
	v_lshlrev_b32_e32 v0, 10, v182
	v_lshlrev_b32_e32 v10, 10, v184
	v_lshlrev_b32_e32 v12, 10, v186
	v_lshlrev_b32_e32 v14, 10, v188
	v_lshl_add_u64 v[164:165], v[6:7], 0, s[22:23]
	s_mov_b64 s[22:23], 0x8860000
	s_and_b64 s[94:95], s[92:93], vcc
	v_cmp_gt_i32_e32 vcc, 0, v5
	s_movk_i32 s0, 0x400
	v_writelane_b32 v255, s4, 3
	v_mul_f32_e32 v114, 0, v115
	v_lshlrev_b32_e32 v142, 10, v194
	v_lshlrev_b32_e32 v132, 11, v146
	v_mov_b32_e32 v133, v1
	v_lshlrev_b32_e32 v154, 3, v131
	v_mov_b32_e32 v195, v1
	v_lshlrev_b32_e32 v155, 4, v131
	v_and_b32_e32 v160, 56, v130
	v_lshlrev_b32_e32 v183, 7, v182
	v_lshlrev_b32_e32 v185, 7, v184
	v_lshlrev_b32_e32 v187, 7, v186
	v_lshlrev_b32_e32 v189, 7, v188
	v_mov_b32_e32 v162, v116
	v_mov_b32_e32 v163, v116
	v_lshl_add_u32 v161, v232, 2, v239
	v_lshlrev_b32_e32 v174, 5, v3
	v_lshlrev_b32_e32 v175, 10, v178
	v_lshl_add_u64 v[166:167], v[8:9], 0, s[22:23]
	v_lshlrev_b32_e32 v168, 1, v2
	v_lshlrev_b32_e32 v170, 1, v4
	v_lshlrev_b32_e32 v0, 1, v0
	v_lshlrev_b32_e32 v134, 1, v10
	v_lshlrev_b32_e32 v136, 1, v12
	v_lshlrev_b32_e32 v138, 1, v14
	s_and_b64 s[96:97], s[94:95], vcc
	s_sub_i32 s72, 0, s73
	v_cmp_gt_i32_e64 s[0:1], s0, v232
	v_cmp_gt_i32_e64 s[6:7], 59, v5
	v_writelane_b32 v255, s5, 4
	s_mov_b64 s[4:5], -1
	s_branch .LBB0_278

; #define ATT_WAIT_BAR(N) asm volatile("s_waitcnt vmcnt(" #N ") lgkmcnt(0)\n\ts_barrier" ::: "memory")
; #define ATT_DMA(t, slot) do { glds16(ksrc + (long)(t) * tstep, (unsigned)__builtin_amdgcn_readfirstlane(kdst + (slot))); glds16(vsrc + (long)(t) * tstep, (unsigned)__builtin_amdgcn_readfirstlane(vdst + (slot))); } while (0)
; template <class BIAS>
; __device__ __forceinline__ void attn_tiles(char* shm, const UnitIO& io, int t_begin, int t_end, const BIAS& B, int tid) {
;     ...
;     bf16x8 qr[4];
;     { const bf16* qp = io.Q + (long)r32 * io.qstride + hi * 8;
; #pragma unroll
;       for (int d0 = 0; d0 < 4; ++d0) qr[d0] = *reinterpret_cast<const bf16x8*>(qp + d0 * 16); }
;     ATT_DMA(t_begin, 0);
;     asm volatile("" :: "v"(qr[0]), "v"(qr[1]), "v"(qr[2]), "v"(qr[3]));
;     const int nt_ = t_end - t_begin; if (nt_ > 1) ATT_DMA(t_begin + 1, SLOTB); if (nt_ > 2) ATT_DMA(t_begin + 2, 2 * SLOTB);
;     f32x16 o[2]; o[0] = f32x16{}; o[1] = f32x16{}; float l_reg = 0.f;
;     if (nt_ > 2) ATT_WAIT_BAR(4); else if (nt_ > 1) ATT_WAIT_BAR(2); else ATT_WAIT_BAR(0);
; __device__ __forceinline__ void moba_unit(Frame& F, const AttnBufs& A, int b, int h, int qb) {
;     ...
;     unsigned selmask = 0u; if (i0 >= 0) selmask |= 1u << i0; if (i1 >= 0) selmask |= 1u << i1; if (i2 >= 0) selmask |= 1u << i2;
.LBB0_294:
	v_lshlrev_b32_e64 v2, v41, 1
	v_cmp_lt_i32_e32 vcc, -1, v41
	v_lshlrev_b32_e64 v3, v5, 1
	v_lshlrev_b32_e32 v148, 1, v154
	v_cndmask_b32_e32 v2, 0, v2, vcc
	v_cmp_lt_i32_e32 vcc, -1, v5
	v_lshlrev_b32_e64 v5, v4, 1
	v_mov_b32_e32 v149, v1
	v_cndmask_b32_e32 v3, 0, v3, vcc
	v_cmp_lt_i32_e32 vcc, -1, v4
	v_readfirstlane_b32 s27, v232
	s_ashr_i32 s16, s27, 6
	v_cndmask_b32_e32 v4, 0, v5, vcc
	v_or3_b32 v135, v3, v2, v4
	v_add_u32_e32 v2, s22, v143
	v_cvt_f32_i32_e32 v137, v2
	v_lshl_add_u64 v[2:3], s[4:5], 0, v[132:133]
	v_lshl_add_u64 v[2:3], v[2:3], 0, v[148:149]
	flat_load_dwordx4 v[66:69], v[2:3]
	flat_load_dwordx4 v[70:73], v[2:3] offset:32
	flat_load_dwordx4 v[74:77], v[2:3] offset:64
	flat_load_dwordx4 v[78:81], v[2:3] offset:96
	s_lshl_b32 s12, s16, 4
	v_and_or_b32 v4, s12, 48, v178
	s_ashr_i32 s12, s27, 3
	s_lshl_b32 s14, s16, 3
	s_andn2_b32 s12, s12, 31
	s_ashr_i32 s15, s14, 31
	s_ashr_i32 s13, s12, 31
	v_lshlrev_b32_e32 v4, 11, v4
	v_mov_b32_e32 v5, v1
	s_lshl_b64 s[4:5], s[14:15], 1
	v_lshl_add_u64 v[4:5], s[30:31], 0, v[4:5]
	s_lshl_b64 s[12:13], s[12:13], 1
	s_lshl_b32 s29, s16, 10
	v_lshl_add_u64 v[2:3], v[156:157], 0, s[4:5]
	v_lshl_add_u64 v[2:3], v[2:3], 0, v[244:245]
	v_lshl_add_u64 v[4:5], v[4:5], 0, s[12:13]
	v_lshlrev_b32_e32 v150, 1, v144
	v_mov_b32_e32 v151, v1
	s_mov_b32 s14, m0
	s_mov_b32 m0, s29
	s_nop 0
	global_load_lds_dwordx4 v[2:3], off
	s_mov_b32 m0, s14
	s_add_i32 s33, s29, 0x8000
	v_lshl_add_u64 v[4:5], v[4:5], 0, v[150:151]
	s_mov_b32 s14, m0
	s_mov_b32 m0, s33
	s_nop 0
	global_load_lds_dwordx4 v[4:5], off
	s_mov_b32 m0, s14
	s_mov_b64 s[22:23], 0x20000
	s_add_i32 s14, s29, 0x2000
	v_lshl_add_u64 v[6:7], v[2:3], 0, s[22:23]
	v_mov_b32_e32 v16, v1
	v_mov_b32_e32 v17, v1
	s_lshl_b32 s26, s20, 2
	v_mov_b32_e32 v8, v1
	v_mov_b32_e32 v9, v1
	v_mov_b32_e32 v10, v1
	v_mov_b32_e32 v11, v1
	v_mov_b32_e32 v12, v1
	v_mov_b32_e32 v13, v1
	v_mov_b32_e32 v14, v1
	v_mov_b32_e32 v15, v1
	s_lshl_b64 s[10:11], s[10:11], 10
	s_mov_b32 s17, 0
	s_add_i32 s28, s26, 4
	v_lshl_add_u64 v[172:173], v[166:167], 0, s[4:5]
	v_lshl_add_u64 v[172:173], v[172:173], 0, v[244:245]
	s_sub_i32 s20, 0, s26
	s_sub_i32 s24, s72, s26
	v_mov_b32_e32 v139, 0
	v_mov_b32_e32 v149, v145
	s_waitcnt vmcnt(0) lgkmcnt(0)
	s_mov_b32 s15, m0
	s_mov_b32 m0, s14
	s_nop 0
	global_load_lds_dwordx4 v[6:7], off
	s_mov_b32 m0, s15
	s_add_i32 s14, s33, 0x2000
	v_lshl_add_u64 v[6:7], v[4:5], 0, s[22:23]
	s_mov_b32 s15, m0
	s_mov_b32 m0, s14
	s_nop 0
	global_load_lds_dwordx4 v[6:7], off
	s_mov_b32 m0, s15
	s_mov_b64 s[22:23], 0x40000
	s_add_i32 s14, s29, 0x4000
	v_lshl_add_u64 v[2:3], v[2:3], 0, s[22:23]
	s_mov_b32 s15, m0
	s_mov_b32 m0, s14
	s_nop 0
	global_load_lds_dwordx4 v[2:3], off
	s_mov_b32 m0, s15
	s_add_i32 s14, s33, 0x4000
	v_lshl_add_u64 v[2:3], v[4:5], 0, s[22:23]
	s_mov_b32 s15, m0
	s_mov_b32 m0, s14
	s_nop 0
	global_load_lds_dwordx4 v[2:3], off
	s_mov_b32 m0, s15
	s_lshl_b32 s14, s16, 15
	s_and_b32 s14, s14, 0x18000
	v_lshl_or_b32 v2, v175, 1, s14
	v_mov_b32_e32 v3, v1
	s_waitcnt vmcnt(4) lgkmcnt(0)
	s_barrier
	v_lshl_add_u64 v[2:3], s[12:13], 0, v[2:3]
	v_lshl_add_u64 v[152:153], v[164:165], 0, v[2:3]
	v_mov_b32_e32 v2, v1
	v_mov_b32_e32 v3, v1
	v_mov_b32_e32 v4, v1
	v_mov_b32_e32 v5, v1
	v_mov_b32_e32 v6, v1
	v_mov_b32_e32 v7, v1
	v_mov_b64_e32 v[32:33], v[16:17]
	s_movk_i32 s22, 0x6000
	v_mov_b64_e32 v[30:31], v[14:15]
	v_mov_b64_e32 v[28:29], v[12:13]
	v_mov_b64_e32 v[26:27], v[10:11]
	v_mov_b64_e32 v[24:25], v[8:9]
	v_mov_b64_e32 v[22:23], v[6:7]
	v_mov_b64_e32 v[20:21], v[4:5]
	v_mov_b64_e32 v[18:19], v[2:3]
	s_branch .LBB0_296

; #define ATT_SBAR() __builtin_amdgcn_sched_barrier(0)
;     __device__ __forceinline__ void init(f32x16& c0, f32x16& c1, int t) const {
;         float base = slope2 * ((float)(64 * t + 4 * hi) - tqf);
;         if (t < nb0) { if (!((selmask >> (t >> 2)) & 1u)) base = ATT_NEG; }
;         const float d32 = 32.0f * slope2;
; #pragma unroll
;         for (int i = 0; i < 8; ++i) { const int r = 2 * i; const f32x2_t kc = (f32x2_t){slope2 * (float)((r & 3) + 8 * (r >> 2)), slope2 * (float)(((r + 1) & 3) + 8 * ((r + 1) >> 2))};
;             const f32x2_t p = kc + base, q = p + d32; c0[r] = p[0]; c0[r + 1] = p[1]; c1[r] = q[0]; c1[r + 1] = q[1]; }
; template <class BIAS>
; __device__ __forceinline__ void attn_tiles(char* shm, const UnitIO& io, int t_begin, int t_end, const BIAS& B, int tid) {
;     ...
;         u32x4 pw[4]; f32x16 c1x;
;         if (act) {
;             bf16x8 kf[8]; const lds_cptr kp = kp0 + sl_c;
; #pragma unroll
;             for (int j = 0; j < 4; ++j) { kf[2 * j] = *(const __attribute__((address_space(3))) bf16x8*)(kp + j * 2048); kf[2 * j + 1] = *(const __attribute__((address_space(3))) bf16x8*)(kp + j * 2048 + 512); }
;             ATT_SBAR();
;             f32x16 c0, c1; B.init(c0, c1, t);
.LBB0_298:
	s_add_i32 s34, s20, s17
	s_cmp_lt_u32 s17, s26
	s_cselect_b64 s[14:15], -1, 0
	s_cmp_le_i32 s34, s73
	s_cselect_b64 s[4:5], -1, 0
	s_or_b64 vcc, s[14:15], s[4:5]
	s_add_i32 s4, s22, 0xffffa000
	v_cndmask_b32_e64 v58, 0, 1, vcc
	s_and_b32 s23, s4, 0x6000
	v_cmp_ne_u32_e64 s[4:5], 1, v58
	s_andn2_b64 vcc, exec, vcc
	s_cbranch_vccnz .Lmo_inact
	v_add_u32_e32 v34, s23, v240
	v_add_u32_e32 v35, s23, v241
	v_add_u32_e32 v36, s23, v242
	v_add_u32_e32 v37, s23, v243
	ds_read_b128 v[98:101], v34
	ds_read_b128 v[94:97], v34 offset:4096
	ds_read_b128 v[102:105], v35
	ds_read_b128 v[90:93], v35 offset:4096
	ds_read_b128 v[106:109], v36
	ds_read_b128 v[86:89], v36 offset:4096
	ds_read_b128 v[110:113], v37
	ds_read_b128 v[82:85], v37 offset:4096
	s_add_i32 s35, s24, s17
	v_cvt_f32_u32_e32 v34, v149
	s_lshr_b32 vcc_lo, s17, 2
	s_lshl_b32 vcc_lo, 1, vcc_lo
	v_and_b32_e32 v35, vcc_lo, v135
	v_sub_f32_e32 v34, v34, v137
	v_cmp_eq_u32_e32 vcc, 0, v35
	v_mul_f32_e32 v34, v115, v34
	s_and_b64 vcc, s[14:15], vcc
	v_cndmask_b32_e32 v34, v34, v226, vcc
	v_add_f32_e32 v50, v114, v34
	v_add_f32_e32 v51, v115, v34
	v_add_f32_e32 v52, v118, v34
	v_add_f32_e32 v53, v119, v34
	v_add_f32_e32 v54, v120, v34
	v_add_f32_e32 v55, v121, v34
	v_add_f32_e32 v56, v122, v34
	v_add_f32_e32 v57, v123, v34
	v_add_f32_e32 v58, v124, v34
	v_add_f32_e32 v59, v125, v34
	v_add_f32_e32 v60, v126, v34
	v_add_f32_e32 v61, v127, v34
	v_add_f32_e32 v62, v128, v34
	v_add_f32_e32 v63, v129, v34
	v_add_f32_e32 v64, v140, v34
	v_add_f32_e32 v65, v141, v34
	v_mov_b32_e32 v117, v116
	v_add_f32_e32 v48, v116, v64
	v_add_f32_e32 v49, v117, v65
	v_add_f32_e32 v46, v116, v62
	v_add_f32_e32 v47, v117, v63
	v_add_f32_e32 v44, v116, v60
	v_add_f32_e32 v45, v117, v61
	v_add_f32_e32 v42, v116, v58
	v_add_f32_e32 v43, v117, v59
	v_add_f32_e32 v40, v116, v56
	v_add_f32_e32 v41, v117, v57
	v_add_f32_e32 v38, v116, v54
	v_add_f32_e32 v39, v117, v55
	v_add_f32_e32 v36, v116, v52
	v_add_f32_e32 v37, v117, v53
	s_cmp_lg_u32 s35, 0
	v_add_f32_e32 v34, v162, v50
	v_add_f32_e32 v35, v163, v51
	s_cbranch_scc1 .LBB0_303
	v_cndmask_b32_e64 v48, v48, v226, s[36:37]
	v_cndmask_b32_e64 v47, v47, v226, s[40:41]
	v_cndmask_b32_e64 v46, v46, v226, s[42:43]
	v_cndmask_b32_e64 v45, v45, v226, s[44:45]
	v_cndmask_b32_e64 v44, v44, v226, s[46:47]
	v_cndmask_b32_e64 v43, v43, v226, s[48:49]
	v_cndmask_b32_e64 v42, v42, v226, s[50:51]
	v_cndmask_b32_e64 v41, v41, v226, s[52:53]
	v_cndmask_b32_e64 v40, v40, v226, s[54:55]
	v_cndmask_b32_e64 v39, v39, v226, s[56:57]
	v_cndmask_b32_e64 v38, v38, v226, s[58:59]
	v_cndmask_b32_e64 v37, v37, v226, s[60:61]
	v_cndmask_b32_e64 v36, v36, v226, s[62:63]
	v_cndmask_b32_e64 v35, v35, v226, s[64:65]
	v_cndmask_b32_e64 v34, v34, v226, s[66:67]
	s_and_saveexec_b64 s[14:15], s[6:7]
	s_mov_b32 s35, 0xff800000
	v_mov_b32_e32 v49, s35
	s_or_b64 exec, exec, s[14:15]
	v_cndmask_b32_e64 v65, v65, v226, s[38:39]
	v_cndmask_b32_e64 v50, v50, v226, s[96:97]
	v_cndmask_b32_e64 v51, v51, v226, s[94:95]
	v_cndmask_b32_e64 v52, v52, v226, s[92:93]
	v_cndmask_b32_e64 v53, v53, v226, s[90:91]
	v_cndmask_b32_e64 v54, v54, v226, s[88:89]
	v_cndmask_b32_e64 v55, v55, v226, s[2:3]
	v_cndmask_b32_e64 v56, v56, v226, s[84:85]
	v_cndmask_b32_e64 v57, v57, v226, s[82:83]
	v_cndmask_b32_e64 v58, v58, v226, s[80:81]
	v_cndmask_b32_e64 v59, v59, v226, s[78:79]
	v_cndmask_b32_e64 v60, v60, v226, s[76:77]
	v_cndmask_b32_e64 v61, v61, v226, s[74:75]
	v_cndmask_b32_e64 v62, v62, v226, s[18:19]
	v_cndmask_b32_e64 v63, v63, v226, s[70:71]
	v_cndmask_b32_e64 v64, v64, v226, s[68:69]

; #define ATT_WAIT_BAR(N) asm volatile("s_waitcnt vmcnt(" #N ") lgkmcnt(0)\n\ts_barrier" ::: "memory")
; #define ATT_DMA(t, slot) do { glds16(ksrc + (long)(t) * tstep, (unsigned)__builtin_amdgcn_readfirstlane(kdst + (slot))); glds16(vsrc + (long)(t) * tstep, (unsigned)__builtin_amdgcn_readfirstlane(vdst + (slot))); } while (0)
; template <class BIAS>
; __device__ __forceinline__ void attn_tiles(char* shm, const UnitIO& io, int t_begin, int t_end, const BIAS& B, int tid) {
;     ...
;     bf16x8 qr[4];
;     { const bf16* qp = io.Q + (long)r32 * io.qstride + hi * 8;
; #pragma unroll
;       for (int d0 = 0; d0 < 4; ++d0) qr[d0] = *reinterpret_cast<const bf16x8*>(qp + d0 * 16); }
;     ATT_DMA(t_begin, 0);
;     asm volatile("" :: "v"(qr[0]), "v"(qr[1]), "v"(qr[2]), "v"(qr[3]));
;     const int nt_ = t_end - t_begin; if (nt_ > 1) ATT_DMA(t_begin + 1, SLOTB); if (nt_ > 2) ATT_DMA(t_begin + 2, 2 * SLOTB);
;     f32x16 o[2]; o[0] = f32x16{}; o[1] = f32x16{}; float l_reg = 0.f;
;     if (nt_ > 2) ATT_WAIT_BAR(4); else if (nt_ > 1) ATT_WAIT_BAR(2); else ATT_WAIT_BAR(0);
; __device__ __forceinline__ void fox_unit(Frame& F, const AttnBufs& A, int b, int h, int qb) {
;     ...
;     { bool skip = false; if (lane < nb0) skip = (c_first - CS[64 * lane + 63]) < -70.0f;
;       const unsigned long long bm = __ballot(skip); t_begin = (int)__builtin_ctzll(~bm); if (t_begin > nb0) t_begin = nb0; }
;     t_begin = __builtin_amdgcn_readfirstlane(t_begin);
;     att::BiasFox B; B.cs2 = CS; B.qrel = w * 32 + r32; B.base = CS[qb * 256 + B.qrel]; B.hi = hi; B.w = w; B.nb0 = nb0; B.u = 32 * (w & 1) + r32 - 4 * hi;
;     const size_t row0 = (size_t)b * SEQ + qb * 256 + w * 32;
;     const size_t bo = (size_t)b * BADJ;
;     att::UnitIO io; io.Q = A.Q + bo + row0 * DM + h * 64; io.qstride = DM; io.K0 = A.K + bo + (size_t)b * SEQ * DM + h * 64; io.V0 = A.V + bo + (size_t)b * SEQ * DM + h * 64; io.kstride = DM;
.LBB0_327:
	s_or_b64 exec, exec, s[34:35]
	v_cndmask_b32_e64 v2, 0, 1, s[42:43]
	v_cmp_ne_u32_e32 vcc, 0, v2
	s_not_b64 s[26:27], vcc
	s_ff1_i32_b64 s21, s[26:27]
	s_min_u32 s34, s51, s21
	v_readlane_b32 s21, v254, 36
	v_lshl_add_u32 v2, s20, 2, v162
	s_add_u32 s42, s21, s20
	v_readlane_b32 s20, v254, 40
	s_addc_u32 s43, s20, 0
	s_lshl_b64 s[20:21], s[42:43], 11
	v_readlane_b32 s22, v254, 42
	s_add_u32 s20, s22, s20
	v_readlane_b32 s22, v254, 45
	s_addc_u32 s21, s22, s21
	s_lshl_b32 s38, s53, 7
	s_add_u32 s20, s20, s38
	s_addc_u32 s21, s21, 0
	v_lshl_add_u64 v[4:5], s[20:21], 0, v[132:133]
	v_mov_b32_e32 v149, v1
	v_lshl_add_u64 v[4:5], v[4:5], 0, v[148:149]
	ds_read_b32 v2, v2
	flat_load_dwordx4 v[82:85], v[4:5] offset:512
	flat_load_dwordx4 v[86:89], v[4:5] offset:544
	flat_load_dwordx4 v[90:93], v[4:5] offset:576
	flat_load_dwordx4 v[94:97], v[4:5] offset:608
	v_readlane_b32 s22, v254, 9
	v_readlane_b32 s22, v254, 55
	s_add_u32 s44, s22, s38
	v_readlane_b32 s22, v254, 57
	v_readfirstlane_b32 s55, v232
	v_readlane_b32 s23, v254, 10
	s_addc_u32 s45, s22, 0
	s_ashr_i32 s54, s55, 6
	s_mov_b32 s39, s23
	s_lshl_b32 s36, s54, 3
	s_lshl_b32 s22, s54, 4
	s_ashr_i32 s37, s36, 31
	v_and_or_b32 v3, s22, 48, v178
	s_ashr_i32 s22, s55, 3
	v_lshl_add_u64 v[4:5], v[140:141], 0, s[38:39]
	s_and_b32 s46, s22, 0xffffffe0
	v_lshl_add_u64 v[144:145], s[36:37], 1, v[4:5]
	v_lshl_add_u64 v[144:145], v[144:145], 0, v[244:245]
	v_lshlrev_b32_e32 v4, 11, v3
	v_mov_b32_e32 v5, v1
	s_ashr_i32 s47, s46, 31
	v_lshl_add_u64 v[4:5], s[44:45], 0, v[4:5]
	s_ashr_i32 s35, s34, 31
	v_lshl_add_u64 v[4:5], s[46:47], 1, v[4:5]
	v_mov_b32_e32 v151, v1
	s_lshl_b64 s[44:45], s[34:35], 17
	s_mov_b32 s21, s23
	v_lshl_add_u64 v[154:155], v[4:5], 0, v[150:151]
	v_lshl_add_u64 v[4:5], v[144:145], 0, s[44:45]
	s_mov_b64 s[22:23], 0x200
	v_writelane_b32 v254, s20, 9
	v_lshl_add_u64 v[4:5], v[4:5], 0, s[22:23]
	s_lshl_b32 s27, s54, 10
	v_writelane_b32 v254, s21, 10
	s_mov_b32 s20, m0
	s_mov_b32 m0, s27
	s_nop 0
	global_load_lds_dwordx4 v[4:5], off
	s_mov_b32 m0, s20
	v_lshl_add_u64 v[4:5], v[154:155], 0, s[44:45]
	s_add_i32 s26, s51, 4
	s_add_i32 s33, s27, 0x8000
	v_lshl_add_u64 v[4:5], v[4:5], 0, s[22:23]
	s_mov_b32 s20, m0
	s_mov_b32 m0, s33
	s_nop 0
	global_load_lds_dwordx4 v[4:5], off
	s_mov_b32 m0, s20
	s_sub_i32 s20, s26, s34
	s_cmp_lt_i32 s20, 2
	s_cselect_b64 s[46:47], -1, 0
	s_and_b64 vcc, exec, s[46:47]
	s_waitcnt vmcnt(0) lgkmcnt(0)
	s_cbranch_vccnz .LBB0_332
	s_add_u32 s36, s44, 0x20000
	s_addc_u32 s37, s45, 0
	v_lshl_add_u64 v[4:5], v[144:145], 0, s[36:37]
	s_mov_b64 s[38:39], 0x200
	v_lshl_add_u64 v[4:5], v[4:5], 0, s[38:39]
	s_add_i32 s21, s27, 0x2000
	s_mov_b32 s22, m0
	s_mov_b32 m0, s21
	s_nop 0
	global_load_lds_dwordx4 v[4:5], off
	s_mov_b32 m0, s22
	v_lshl_add_u64 v[4:5], v[154:155], 0, s[36:37]
	v_lshl_add_u64 v[4:5], v[4:5], 0, s[38:39]
	s_add_i32 s21, s33, 0x2000
	s_mov_b32 s22, m0
	s_mov_b32 m0, s21
	s_nop 0
	global_load_lds_dwordx4 v[4:5], off
	s_mov_b32 m0, s22
	s_cmp_lt_i32 s20, 3
	s_mov_b64 s[44:45], -1
	s_cbranch_scc1 .LBB0_333

; #define ATT_SBAR() __builtin_amdgcn_sched_barrier(0)
; #define ATT_DMA(t, slot) do { glds16(ksrc + (long)(t) * tstep, (unsigned)__builtin_amdgcn_readfirstlane(kdst + (slot))); glds16(vsrc + (long)(t) * tstep, (unsigned)__builtin_amdgcn_readfirstlane(vdst + (slot))); } while (0)
;     __device__ __forceinline__ void init(f32x16& c0, f32x16& c1, int t) const {
;         const lds_fptr p = cs2 + 64 * t + 4 * hi;
;         f32x4 a[4], b[4];
; #pragma unroll
;         for (int g = 0; g < 4; ++g) { a[g] = *(const __attribute__((address_space(3))) f32x4*)(p + 8 * g); b[g] = *(const __attribute__((address_space(3))) f32x4*)(p + 32 + 8 * g); }
;         asm volatile("" : "+v"(a[0]), "+v"(a[1]), "+v"(a[2]), "+v"(a[3]), "+v"(b[0]), "+v"(b[1]), "+v"(b[2]), "+v"(b[3]));
; #pragma unroll
;         for (int g = 0; g < 4; ++g) { const f32x2_t a0 = (f32x2_t){a[g][0], a[g][1]}, a1 = (f32x2_t){a[g][2], a[g][3]}, b0 = (f32x2_t){b[g][0], b[g][1]}, b1 = (f32x2_t){b[g][2], b[g][3]};
;             const f32x2_t x0 = base - a0, x1 = base - a1, y0 = base - b0, y1 = base - b1;
;             c0[4 * g] = x0[0]; c0[4 * g + 1] = x0[1]; c0[4 * g + 2] = x1[0]; c0[4 * g + 3] = x1[1]; c1[4 * g] = y0[0]; c1[4 * g + 1] = y0[1]; c1[4 * g + 2] = y1[0]; c1[4 * g + 3] = y1[1]; }
;         if (t - nb0 == (w >> 1)) {
; #pragma unroll
;             for (int r = 0; r < 16; ++r) { const int ko = (r & 3) + 8 * (r >> 2); if (ko > u) c0[r] = ATT_NEG; if (ko > u - 32) c1[r] = ATT_NEG; }
;         }
; template <class BIAS>
; __device__ __forceinline__ void attn_tiles(char* shm, const UnitIO& io, int t_begin, int t_end, const BIAS& B, int tid) {
;     ...
;         const int rem = t_end - t;
;         const bool act = B.active(t);
;         const int sl_c = ((t - t_begin) & 3) * SLOTB;
;         if (rem > 3) ATT_DMA(t + 3, ((t + 3 - t_begin) & 3) * SLOTB);
;         u32x4 pw[4]; f32x16 c1x;
;         if (act) {
;             bf16x8 kf[8]; const lds_cptr kp = kp0 + sl_c;
; #pragma unroll
;             for (int j = 0; j < 4; ++j) { kf[2 * j] = *(const __attribute__((address_space(3))) bf16x8*)(kp + j * 2048); kf[2 * j + 1] = *(const __attribute__((address_space(3))) bf16x8*)(kp + j * 2048 + 512); }
;             ATT_SBAR();
;             f32x16 c0, c1; B.init(c0, c1, t);
.LBB0_341:
.LBB0_342:
	s_add_i32 s20, s44, -3
	s_add_i32 s45, s37, s44
	s_cmp_lt_i32 s20, s51
	s_cselect_b64 s[20:21], -1, 0
	s_add_i32 s22, s45, -3
	s_cmp_le_i32 s22, s73
	s_cselect_b64 s[34:35], -1, 0
	s_or_b64 vcc, s[20:21], s[34:35]
	s_add_i32 s20, s39, 0xffffa000
	v_cndmask_b32_e64 v74, 0, 1, vcc
	s_and_b32 s20, s20, 0x6000
	v_cmp_ne_u32_e64 s[34:35], 1, v74
	s_andn2_b64 vcc, exec, vcc
	s_cbranch_vccnz .Lfx_inact
	v_add_u32_e32 v50, s20, v240
	v_add_u32_e32 v51, s20, v241
	v_add_u32_e32 v52, s20, v242
	v_add_u32_e32 v53, s20, v243
	ds_read_b128 v[114:117], v50
	ds_read_b128 v[110:113], v50 offset:4096
	ds_read_b128 v[118:121], v51
	ds_read_b128 v[106:109], v51 offset:4096
	ds_read_b128 v[122:125], v52
	ds_read_b128 v[102:105], v52 offset:4096
	ds_read_b128 v[126:129], v53
	ds_read_b128 v[98:101], v53 offset:4096
	s_add_i32 s21, s36, s44
	ds_read_b128 v[50:53], v137 offset:224
	ds_read_b128 v[54:57], v137 offset:192
	ds_read_b128 v[58:61], v137 offset:96
	ds_read_b128 v[62:65], v137 offset:64
	ds_read_b128 v[218:221], v137 offset:160
	ds_read_b128 v[234:237], v137 offset:128
	ds_read_b128 v[66:69], v137
	ds_read_b128 v[70:73], v137 offset:32
	s_cmp_lg_u32 s21, 3
	s_waitcnt lgkmcnt(0)
	s_nop 0
	v_sub_f32_e32 v81, v33, v61
	v_sub_f32_e32 v80, v32, v60
	v_sub_f32_e32 v79, v31, v59
	v_sub_f32_e32 v78, v30, v58
	v_sub_f32_e32 v77, v29, v65
	v_sub_f32_e32 v76, v28, v64
	v_sub_f32_e32 v75, v11, v63
	v_sub_f32_e32 v74, v10, v62
	v_sub_f32_e32 v73, v9, v73
	v_sub_f32_e32 v72, v8, v72
	v_sub_f32_e32 v71, v7, v71
	v_sub_f32_e32 v70, v6, v70
	v_sub_f32_e32 v69, v5, v69
	v_sub_f32_e32 v68, v4, v68
	v_sub_f32_e32 v67, v3, v67
	v_sub_f32_e32 v66, v2, v66
	v_sub_f32_e32 v65, v33, v53
	v_sub_f32_e32 v64, v32, v52
	v_sub_f32_e32 v63, v31, v51
	v_sub_f32_e32 v62, v30, v50
	v_sub_f32_e32 v61, v29, v57
	v_sub_f32_e32 v60, v28, v56
	v_sub_f32_e32 v59, v11, v55
	v_sub_f32_e32 v58, v10, v54
	v_sub_f32_e32 v57, v9, v221
	v_sub_f32_e32 v56, v8, v220
	v_sub_f32_e32 v55, v7, v219
	v_sub_f32_e32 v54, v6, v218
	v_sub_f32_e32 v53, v5, v237
	v_sub_f32_e32 v52, v4, v236
	v_sub_f32_e32 v51, v3, v235
	v_sub_f32_e32 v50, v2, v234
	s_cbranch_scc1 .LBB0_347
	v_cndmask_b32_e64 v64, v64, v226, s[56:57]
	v_cndmask_b32_e64 v63, v63, v226, s[60:61]
	v_cndmask_b32_e64 v62, v62, v226, s[62:63]
	v_cndmask_b32_e64 v61, v61, v226, s[64:65]
	v_cndmask_b32_e64 v60, v60, v226, s[66:67]
	v_cndmask_b32_e64 v59, v59, v226, s[0:1]
	v_cndmask_b32_e64 v58, v58, v226, s[40:41]
	v_cndmask_b32_e64 v57, v57, v226, s[68:69]
	v_cndmask_b32_e64 v56, v56, v226, s[70:71]
	v_cndmask_b32_e64 v55, v55, v226, s[48:49]
	v_cndmask_b32_e64 v54, v54, v226, s[74:75]
	v_cndmask_b32_e64 v53, v53, v226, s[76:77]
	v_cndmask_b32_e64 v52, v52, v226, s[78:79]
	v_cndmask_b32_e64 v51, v51, v226, s[80:81]
	v_cndmask_b32_e64 v50, v50, v226, s[82:83]
	s_and_saveexec_b64 vcc, s[30:31]
	s_mov_b32 s21, 0xff800000
	v_mov_b32_e32 v65, s21
	s_or_b64 exec, exec, vcc
	v_cndmask_b32_e64 v81, v81, v226, s[58:59]
	v_cndmask_b32_e64 v80, v80, v226, s[84:85]
	v_cndmask_b32_e64 v79, v79, v226, s[2:3]
	v_cndmask_b32_e64 v78, v78, v226, s[88:89]
	v_cndmask_b32_e64 v77, v77, v226, s[90:91]
	v_cndmask_b32_e64 v76, v76, v226, s[92:93]
	v_cndmask_b32_e64 v75, v75, v226, s[94:95]
	v_cndmask_b32_e64 v74, v74, v226, s[96:97]
	v_cndmask_b32_e64 v73, v73, v226, s[4:5]
	v_cndmask_b32_e64 v72, v72, v226, s[6:7]
	v_cndmask_b32_e64 v71, v71, v226, s[8:9]
	v_cndmask_b32_e64 v70, v70, v226, s[10:11]
	v_cndmask_b32_e64 v69, v69, v226, s[12:13]
	v_cndmask_b32_e64 v68, v68, v226, s[14:15]
	v_cndmask_b32_e64 v67, v67, v226, s[16:17]
	v_cndmask_b32_e64 v66, v66, v226, s[18:19]

; __device__ __forceinline__ void dil_unit(Frame& F, const AttnBufs& A, int b, int h, int g, int r, int c) {
;     char* shm = (char*)F.lds; const int tid = F.tid, lane = tid & 63, r32 = lane & 31, hi = lane >> 5, w = F.wave;
;     const int dil = (g == 0) ? 1 : (g == 1 ? 4 : 16);
;     const int i0 = 256 * c;
;     att::BiasDil B; B.sd = exp2f(-8.0f * (float)(h - 10 + 1) / 10.0f) * LOG2E * (float)dil; B.qrel = 128 + w * 32 + r32; B.hi = hi; B.w = w; B.setup(r32);
;     const long tok_q0 = (long)b * SEQ + r + (long)dil * (i0 + w * 32);
;     const long tok_k0 = (long)b * SEQ + r + (long)dil * (i0 - 128);
;     const long bo = (long)b * (long)BADJ;
;     att::UnitIO io; io.Q = A.Q + bo + tok_q0 * DM + h * 64; io.qstride = (long)DM * dil; io.K0 = A.K + bo + tok_k0 * DM + h * 64; io.V0 = A.V + bo + tok_k0 * DM + h * 64; io.kstride = (long)DM * dil;
;     io.O = A.OD + (size_t)g * OD_BRANCH + tok_q0 * 384 + (h - 10) * 64; io.ostride = (long)384 * dil; io.L = A.LD + (size_t)g * LD_BRANCH + tok_q0 * 8 + (h - 10); io.lstride = (long)8 * dil; io.norm = false;
; __device__ __forceinline__ void attn_phase(Frame& F, const AttnBufs& A) {
;     ...
;     for (int k = 0; k < 9; ++k) { const int idx = r + 32 * k, h6 = idx / 48, rest = idx % 48, br = rest >> 4, i16 = rest & 15;
;         const int rr = (br == 0) ? 0 : (br == 1 ? (i16 >> 2) : i16), c = (br == 0) ? i16 : (br == 1 ? (i16 & 3) : 0);
;         dil_unit(F, A, g, 10 + h6, br, rr, c); }
.LBB0_363:
	s_lshl_b32 s56, s74, 5
	v_readlane_b32 s2, v254, 30
	s_or_b32 s56, s56, s2
	s_mul_hi_u32 s57, s56, 0xaaaaaaab
	s_lshr_b32 s75, s57, 5
	s_mul_i32 s57, s75, 48
	s_sub_i32 s66, s56, s57
	s_lshr_b32 s2, s66, 4
	s_and_b32 s67, s66, 15
	s_cmp_lt_u32 s66, 16
	s_cselect_b64 s[62:63], -1, 0
	s_cmp_eq_u32 s2, 1
	s_cselect_b64 s[64:65], -1, 0
	s_bfe_u32 s68, s66, 0x20002
	s_and_b64 s[56:57], s[64:65], exec
	s_cselect_b32 s68, s68, s67
	s_and_b64 s[56:57], s[62:63], exec
	s_cselect_b32 s68, 0, s68
	s_and_b32 s66, s66, 3
	s_and_b64 s[56:57], s[64:65], exec
	s_cselect_b32 s66, s66, 0
	s_and_b64 s[56:57], s[62:63], exec
	s_cselect_b32 s76, s67, s66
	s_and_b64 s[56:57], s[64:65], exec
	s_cselect_b32 s66, 4, 16
	s_and_b64 s[56:57], s[62:63], exec
	s_cselect_b32 s80, 1, s66
	s_not_b32 s56, s75
	s_lshl_b32 s56, s56, 3
	v_cvt_f32_i32_e32 v0, s56
	s_mov_b32 s84, 0x41200000
	s_mov_b32 s85, 0x41300000
	s_lshl_b32 s69, s76, 8
	v_div_scale_f32 v2, s[56:57], s84, s84, v0
	v_rcp_f32_e32 v3, v2
	s_mov_b32 s56, 0xc2fc0000
	v_readlane_b32 s70, v254, 38
	v_readlane_b32 s71, v254, 39
	v_fma_f32 v4, -v2, v3, 1.0
	v_fmac_f32_e32 v3, v4, v3
	v_div_scale_f32 v4, vcc, v0, s84, v0
	v_mul_f32_e32 v5, v4, v3
	v_fma_f32 v6, -v2, v5, v4
	v_fmac_f32_e32 v5, v6, v3
	v_fma_f32 v2, -v2, v5, v4
	v_div_fmas_f32 v2, v2, v3, v5
	v_div_fixup_f32 v0, v2, s84, v0
	v_cmp_gt_f32_e32 vcc, s56, v0
	s_and_b64 s[56:57], vcc, exec
	v_readlane_b32 s56, v254, 48
	s_cselect_b32 s81, 0xffffffc0, 0
	s_add_i32 s56, s69, s56
	s_or_b32 s68, s70, s68
	s_ashr_i32 s57, s56, 31
	s_and_b64 s[66:67], s[64:65], exec
	s_cselect_b32 s70, 2, 4
	s_and_b64 s[66:67], s[62:63], exec
	s_cselect_b32 s70, 0, s70
	s_lshl_b64 s[56:57], s[56:57], s70
	s_add_u32 s66, s56, s68
	s_addc_u32 s67, s57, s71
	s_add_i32 s56, s69, 0xffffff80
	s_ashr_i32 s57, s56, 31
	s_lshl_b64 s[56:57], s[56:57], s70
	s_add_u32 s56, s56, s68
	s_addc_u32 s57, s57, s71
	s_lshl_b64 s[68:69], s[66:67], 11
	v_readlane_b32 s70, v254, 42
	s_add_u32 s68, s70, s68
	v_readlane_b32 s70, v254, 45
	s_addc_u32 s69, s70, s69
	s_lshl_b32 s70, s75, 6
	s_lshl_b32 s77, s75, 7
	v_writelane_b32 v255, s70, 49
	s_add_u32 s70, s68, s77
	s_addc_u32 s71, s69, 0
	s_lshl_b64 s[68:69], s[56:57], 11
	v_readlane_b32 s56, v254, 49
	s_add_u32 s56, s56, s68
	v_readlane_b32 s57, v254, 50
	s_addc_u32 s57, s57, s69
	s_add_u32 s56, s56, s77
	s_addc_u32 s57, s57, 0
	v_readlane_b32 s78, v254, 53
	s_add_u32 s68, s78, s68
	v_readlane_b32 s78, v254, 54
	s_addc_u32 s69, s78, s69
	s_add_u32 s68, s68, s77
	s_addc_u32 s69, s69, 0
	s_cmp_eq_u32 s76, 0
	v_readfirstlane_b32 s77, v232
	s_cselect_b32 s88, 2, 0
	s_ashr_i32 s76, s77, 6
	s_and_b64 s[78:79], s[64:65], exec
	s_cselect_b32 s82, 12, 14
	s_and_b64 s[78:79], s[62:63], exec
	s_cselect_b32 s83, 10, s82
	v_lshlrev_b64 v[2:3], s83, v[146:147]
	v_lshl_add_u64 v[2:3], v[2:3], 1, s[70:71]
	v_mov_b32_e32 v149, v1
	v_lshl_add_u64 v[2:3], v[2:3], 0, v[148:149]
	flat_load_dwordx4 v[98:101], v[2:3] offset:1280
	flat_load_dwordx4 v[102:105], v[2:3] offset:1312
	flat_load_dwordx4 v[106:109], v[2:3] offset:1344
	flat_load_dwordx4 v[110:113], v[2:3] offset:1376
	v_cndmask_b32_e32 v4, 0, v224, vcc
	v_add_f32_e32 v0, v0, v4
	v_exp_f32_e32 v0, v0
	v_cvt_f32_ubyte0_e32 v3, s80
	s_mov_b32 s78, 2.0
	s_mov_b32 s79, 0x40400000
	v_ldexp_f32 v0, v0, s81
	v_mul_f32_e32 v0, 0x3fb8aa3b, v0
	v_mul_f32_e32 v155, v0, v3
	v_mov_b32_e32 v0, v155
	v_pk_mul_f32 v[158:159], v[0:1], s[78:79] op_sel_hi:[0,1]
	s_mov_b32 s78, 0x41000000
	s_mov_b32 s79, 0x41100000
	v_pk_mul_f32 v[160:161], v[0:1], s[78:79] op_sel_hi:[0,1]
	s_mov_b32 s78, 0x41800000
	s_mov_b32 s79, 0x41880000
	v_pk_mul_f32 v[164:165], v[0:1], s[78:79] op_sel_hi:[0,1]
	s_mov_b32 s78, 0x41900000
	s_mov_b32 s79, 0x41980000
	v_pk_mul_f32 v[166:167], v[0:1], s[78:79] op_sel_hi:[0,1]
	s_mov_b32 s78, 0x41c00000
	s_mov_b32 s79, 0x41c80000
	v_pk_mul_f32 v[168:169], v[0:1], s[78:79] op_sel_hi:[0,1]
	s_mov_b32 s78, 0x41d00000
	s_mov_b32 s79, 0x41d80000
	v_pk_mul_f32 v[170:171], v[0:1], s[78:79] op_sel_hi:[0,1]
	s_lshl_b32 s70, s76, 4
	s_ashr_i32 s79, s77, 3
	v_pk_mul_f32 v[162:163], v[0:1], s[84:85] op_sel_hi:[0,1]
	s_lshl_b32 s80, s76, 3
	s_lshl_b32 s78, s76, 10
	v_and_or_b32 v0, s70, 48, v178
	s_and_b32 s82, s79, 0xffffffe0
	v_lshlrev_b64 v[4:5], s83, v[194:195]
	s_ashr_i32 s81, s80, 31
	s_add_i32 s79, s78, 0x8000
	v_lshlrev_b64 v[6:7], s83, v[0:1]
	s_ashr_i32 s83, s82, 31
	v_lshl_add_u64 v[4:5], v[4:5], 1, s[56:57]
	s_and_b64 s[56:57], s[64:65], exec
	v_lshl_add_u64 v[172:173], s[80:81], 1, v[4:5]
	v_lshlrev_b32_e32 v248, 11, v246
	v_mov_b32_e32 v249, s2
	v_lshlrev_b32_e32 v249, 1, v249
	v_lshlrev_b32_e32 v248, v249, v248
	v_add_u32_e32 v248, v248, v247
	v_ashrrev_i32_e32 v249, 31, v248
	v_lshl_add_u64 v[172:173], v[172:173], 0, v[248:249]
	v_lshl_add_u64 v[4:5], v[6:7], 1, s[68:69]
	s_cselect_b32 s68, 18, 20
	s_and_b64 s[56:57], s[62:63], exec
	s_mov_b32 s89, s3
	s_cselect_b32 s80, 16, s68
	s_mov_b32 s71, s3
	s_or_b32 s70, s88, 1
	s_lshl_b64 s[56:57], s[88:89], s80
	v_mov_b32_e32 v151, v1
	v_lshl_add_u64 v[4:5], s[82:83], 1, v[4:5]
	s_lshl_b64 s[68:69], s[70:71], s80
	s_lshl_b64 s[56:57], s[56:57], 1
	v_lshl_add_u64 v[174:175], v[4:5], 0, v[150:151]
	s_lshl_b64 s[68:69], s[68:69], 1
	v_lshl_add_u64 v[4:5], v[172:173], 0, s[56:57]
	s_mov_b64 s[70:71], 0x500
	v_lshl_add_u64 v[6:7], v[174:175], 0, s[56:57]
	v_lshl_add_u64 v[8:9], v[172:173], 0, s[68:69]
	v_lshl_add_u64 v[4:5], v[4:5], 0, s[70:71]
	s_mov_b32 s56, m0
	s_mov_b32 m0, s78
	s_nop 0
	global_load_lds_dwordx4 v[4:5], off
	s_mov_b32 m0, s56
	s_add_i32 s81, s78, 0x2000
	v_lshl_add_u64 v[6:7], v[6:7], 0, s[70:71]
	v_lshl_add_u64 v[8:9], v[8:9], 0, s[70:71]
	s_mov_b32 s56, m0
	s_mov_b32 m0, s79
	s_nop 0
	global_load_lds_dwordx4 v[6:7], off
	s_mov_b32 m0, s56
	s_waitcnt vmcnt(0) lgkmcnt(0)
	s_mov_b32 s56, m0
	s_mov_b32 m0, s81
	s_nop 0
	global_load_lds_dwordx4 v[8:9], off
	s_mov_b32 m0, s56
	v_lshl_add_u64 v[4:5], v[174:175], 0, s[68:69]
	v_lshl_add_u64 v[4:5], v[4:5], 0, s[70:71]
	s_add_i32 s56, s79, 0x2000
	s_mov_b32 s57, m0
	s_mov_b32 m0, s56
	s_nop 0
	global_load_lds_dwordx4 v[4:5], off
	s_mov_b32 m0, s57
	s_add_i32 s56, s88, 2
	v_writelane_b32 v254, s2, 9
	s_mov_b32 s57, s3
	s_lshl_b64 s[56:57], s[56:57], s80
	s_lshl_b64 s[56:57], s[56:57], 1
	v_lshl_add_u64 v[4:5], v[172:173], 0, s[56:57]
	v_lshl_add_u64 v[4:5], v[4:5], 0, s[70:71]
	s_add_i32 s68, s78, 0x4000
	s_mov_b32 s69, m0
	s_mov_b32 m0, s68
	s_nop 0
	global_load_lds_dwordx4 v[4:5], off
	s_mov_b32 m0, s69
	v_lshl_add_u64 v[4:5], v[174:175], 0, s[56:57]
	v_mov_b32_e32 v2, 0
	v_lshl_add_u64 v[4:5], v[4:5], 0, s[70:71]
	s_add_i32 s56, s79, 0x4000
	s_mov_b32 s57, m0
	s_mov_b32 m0, s56
	s_nop 0
	global_load_lds_dwordx4 v[4:5], off
	s_mov_b32 m0, s57
	s_waitcnt vmcnt(4) lgkmcnt(0)
	s_barrier
; #pragma unroll
;         for (int i = 0; i < 8; ++i) { const int r = 2 * i; kc[i] = (f32x2_t){sd * (float)((r & 3) + 8 * (r >> 2)), sd * (float)(((r + 1) & 3) + 8 * ((r + 1) >> 2))}; } }
; template <class BIAS>
; __device__ __forceinline__ void attn_tiles(char* shm, const UnitIO& io, int t_begin, int t_end, const BIAS& B, int tid) {
;     ...
;     f32x16 o[2]; o[0] = f32x16{}; o[1] = f32x16{}; float l_reg = 0.f;
	v_mov_b32_e32 v16, v2
	v_mov_b32_e32 v17, v2
	v_mul_f32_e32 v156, 0x42000000, v155
	v_mov_b32_e32 v3, v2
	v_mov_b32_e32 v4, v2
	v_mov_b32_e32 v5, v2
	v_mov_b32_e32 v6, v2
	v_mov_b32_e32 v7, v2
	v_mov_b32_e32 v8, v2
	v_mov_b32_e32 v9, v2
	v_mov_b32_e32 v10, v2
	v_mov_b32_e32 v11, v2
	v_mov_b32_e32 v12, v2
	v_mov_b32_e32 v13, v2
	v_mov_b32_e32 v14, v2
	v_mov_b32_e32 v15, v2
	v_mov_b64_e32 v[32:33], v[16:17]
	v_mul_f32_e32 v149, 0x42800000, v155
	v_mul_f32_e32 v154, 0, v155
	v_writelane_b32 v254, s3, 10
	v_mul_f32_e32 v0, v155, v196
	v_mov_b32_e32 v176, v156
	v_mov_b32_e32 v177, v156
	s_movk_i32 s81, 0x6000
	v_mov_b64_e32 v[30:31], v[14:15]
	v_mov_b64_e32 v[28:29], v[12:13]
	v_mov_b64_e32 v[26:27], v[10:11]
	v_mov_b64_e32 v[24:25], v[8:9]
	v_mov_b64_e32 v[22:23], v[6:7]
	v_mov_b64_e32 v[20:21], v[4:5]
	v_mov_b64_e32 v[18:19], v[2:3]
	v_mov_b32_e32 v151, v2
	s_branch .LBB0_365

; #define ATT_SBAR() __builtin_amdgcn_sched_barrier(0)
; #define ATT_DMA(t, slot) do { glds16(ksrc + (long)(t) * tstep, (unsigned)__builtin_amdgcn_readfirstlane(kdst + (slot))); glds16(vsrc + (long)(t) * tstep, (unsigned)__builtin_amdgcn_readfirstlane(vdst + (slot))); } while (0)
;     __device__ __forceinline__ void init(f32x16& c0, f32x16& c1, int t) const {
;         const int dt = t - (w >> 1);
;         const float base = basel + (float)dt * d64;
; #pragma unroll
;         for (int i = 0; i < 8; ++i) { const f32x2_t p = kc[i] + base, q = p + d32; c0[2 * i] = p[0]; c0[2 * i + 1] = p[1]; c1[2 * i] = q[0]; c1[2 * i + 1] = q[1]; }
;         if (dt == 0) {
; #pragma unroll
;             for (int r = 0; r < 16; ++r) { const int ko = (r & 3) + 8 * (r >> 2); if (ko < u) c0[r] = ATT_NEG; if (ko < u - 32) c1[r] = ATT_NEG; }
;         } else if (dt == 2) {
; #pragma unroll
;             for (int r = 0; r < 16; ++r) { const int ko = (r & 3) + 8 * (r >> 2); if (ko > u) c0[r] = ATT_NEG; if (ko > u - 32) c1[r] = ATT_NEG; }
;         }
; template <class BIAS>
; __device__ __forceinline__ void attn_tiles(char* shm, const UnitIO& io, int t_begin, int t_end, const BIAS& B, int tid) {
;     ...
;     for (int t = t_begin; t < t_end; ++t) {
;         const int rem = t_end - t;
;         const bool act = B.active(t);
;         const int sl_c = ((t - t_begin) & 3) * SLOTB;
;         if (rem > 3) ATT_DMA(t + 3, ((t + 3 - t_begin) & 3) * SLOTB);
;         u32x4 pw[4]; f32x16 c1x;
;         if (act) {
;             bf16x8 kf[8]; const lds_cptr kp = kp0 + sl_c;
; #pragma unroll
;             for (int j = 0; j < 4; ++j) { kf[2 * j] = *(const __attribute__((address_space(3))) bf16x8*)(kp + j * 2048); kf[2 * j + 1] = *(const __attribute__((address_space(3))) bf16x8*)(kp + j * 2048 + 512); }
;             ATT_SBAR();
;             f32x16 c0, c1; B.init(c0, c1, t);
.LBB0_367:
	s_cmp_ge_i32 s88, s73
	s_cselect_b64 s[56:57], -1, 0
	s_cmp_le_i32 s88, s33
	s_cselect_b64 s[70:71], -1, 0
	s_and_b64 s[70:71], s[56:57], s[70:71]
	s_add_i32 s56, s81, 0xffffa000
	v_cndmask_b32_e64 v58, 0, 1, s[70:71]
	s_and_b32 s82, s56, 0x6000
	v_cmp_ne_u32_e64 s[56:57], 1, v58
	s_andn2_b64 vcc, exec, s[70:71]
	s_cbranch_vccnz .Ldl_inact
	v_add_u32_e32 v34, s82, v240
	v_add_u32_e32 v35, s82, v241
	v_add_u32_e32 v36, s82, v242
	v_add_u32_e32 v37, s82, v243
	ds_read_b128 v[130:133], v34
	ds_read_b128 v[126:129], v34 offset:4096
	ds_read_b128 v[134:137], v35
	ds_read_b128 v[122:125], v35 offset:4096
	ds_read_b128 v[138:141], v36
	ds_read_b128 v[118:121], v36 offset:4096
	ds_read_b128 v[142:145], v37
	ds_read_b128 v[114:117], v37 offset:4096
	s_add_u32 s70, s72, s88
	v_cvt_f32_i32_e32 v34, s70
	v_mov_b32_e32 v157, v156
	v_fma_f32 v34, v149, v34, -v0
	v_add_f32_e32 v82, v154, v34
	v_add_f32_e32 v83, v155, v34
	v_add_f32_e32 v84, v158, v34
	v_add_f32_e32 v85, v159, v34
	v_add_f32_e32 v86, v160, v34
	v_add_f32_e32 v87, v161, v34
	v_add_f32_e32 v88, v162, v34
	v_add_f32_e32 v89, v163, v34
	v_add_f32_e32 v90, v164, v34
	v_add_f32_e32 v91, v165, v34
	v_add_f32_e32 v92, v166, v34
	v_add_f32_e32 v93, v167, v34
	v_add_f32_e32 v94, v168, v34
	v_add_f32_e32 v95, v169, v34
	v_add_f32_e32 v96, v170, v34
	v_add_f32_e32 v97, v171, v34
	v_add_f32_e32 v46, v156, v94
	v_add_f32_e32 v47, v157, v95
	v_add_f32_e32 v48, v156, v96
	v_add_f32_e32 v49, v157, v97
	v_add_f32_e32 v44, v156, v92
	v_add_f32_e32 v45, v157, v93
	v_add_f32_e32 v42, v156, v90
	v_add_f32_e32 v43, v157, v91
	v_add_f32_e32 v40, v156, v88
	v_add_f32_e32 v41, v157, v89
	v_add_f32_e32 v38, v156, v86
	v_add_f32_e32 v39, v157, v87
	v_add_f32_e32 v36, v156, v84
	v_add_f32_e32 v37, v157, v85
	v_add_f32_e32 v34, v176, v82
	v_add_f32_e32 v35, v177, v83
	s_cmp_eq_u32 s70, 1
	s_cbranch_scc1 .Ldil_h1_go
	s_cmp_eq_u32 s70, 0
	s_cbranch_scc0 .Ldil_m2
	v_cndmask_b32_e64 v82, v82, v226, s[6:7]
	v_cndmask_b32_e64 v83, v83, v226, s[10:11]
	v_cndmask_b32_e64 v84, v84, v226, s[14:15]
	v_cndmask_b32_e64 v85, v85, v226, s[18:19]
	v_cndmask_b32_e64 v86, v86, v226, s[22:23]
	v_cndmask_b32_e64 v87, v87, v226, s[26:27]
	v_cndmask_b32_e64 v88, v88, v226, s[92:93]
	v_cndmask_b32_e64 v89, v89, v226, s[96:97]
	v_cndmask_b32_e64 v90, v90, v226, s[4:5]
	v_cndmask_b32_e64 v91, v91, v226, s[60:61]
	v_cndmask_b32_e64 v92, v92, v226, s[30:31]
	v_cndmask_b32_e64 v93, v93, v226, s[58:59]
	v_cndmask_b32_e64 v94, v94, v226, s[40:41]
	v_cndmask_b32_e64 v95, v95, v226, s[44:45]
	v_cndmask_b32_e64 v96, v96, v226, s[48:49]
	v_cndmask_b32_e64 v34, v34, v226, s[8:9]
	v_cndmask_b32_e64 v35, v35, v226, s[12:13]
	v_cndmask_b32_e64 v36, v36, v226, s[16:17]
	v_cndmask_b32_e64 v37, v37, v226, s[20:21]
	v_cndmask_b32_e64 v38, v38, v226, s[24:25]
	v_cndmask_b32_e64 v39, v39, v226, s[90:91]
	v_cndmask_b32_e64 v40, v40, v226, s[94:95]
	v_cndmask_b32_e64 v41, v41, v226, s[34:35]
	v_cndmask_b32_e64 v42, v42, v226, s[0:1]
	v_cndmask_b32_e64 v43, v43, v226, s[28:29]
	v_cndmask_b32_e64 v44, v44, v226, s[36:37]
	v_cndmask_b32_e64 v45, v45, v226, s[38:39]
	v_cndmask_b32_e64 v46, v46, v226, s[42:43]
	v_cndmask_b32_e64 v47, v47, v226, s[46:47]
	v_cndmask_b32_e64 v48, v48, v226, s[50:51]
	v_cndmask_b32_e64 v97, v97, v226, s[52:53]
	v_cndmask_b32_e64 v49, v49, v226, s[54:55]
	s_branch .Ldil_h1_go
